# attention unit epilogue: v_permlane32_swap pairs so each half-wave holds a whole 16-byte column group: 8 global_store_dwordx4 per lane instead of 16 dwordx2 (same bytes, same addresses)
# baseline (speedup 1.0000x reference)
; __device__ __forceinline__ unsigned cvt_pk_bf16(float lo, float hi) { const bf16x2_t r = __builtin_convertvector((f32x2_t){lo, hi}, bf16x2_t); return __builtin_bit_cast(unsigned, r); }
; __device__ __forceinline__ void attn_unit(LAS unsigned char* lds, const bf16_t* Q, const bf16_t* K, const bf16_t* Vt, const float* kmean, bf16_t* mix,
;                                           const int b, const int h, const int blk, const int wv) {
;     ...
;     lsum += __shfl_xor(lsum, 32);
;     const float inv = 1.0f / lsum;
;     bf16_t* op = mix + qrow * DM + h * 128 + 4 * hh;
; #pragma unroll
;     for (int d = 0; d < 4; ++d)
; #pragma unroll
;         for (int rg = 0; rg < 4; ++rg) {
;             u32x2 wv; wv[0] = cvt_pk_bf16(o[d][4 * rg] * inv, o[d][4 * rg + 1] * inv); wv[1] = cvt_pk_bf16(o[d][4 * rg + 2] * inv, o[d][4 * rg + 3] * inv);
;             *(u32x2*)(op + 32 * d + 8 * rg) = wv;
;         }
.LBB0_766:
	ds_bpermute_b32 v65, v171, v64
	s_ashr_i32 s0, s22, 3
	s_ashr_i32 s1, s0, 31
	s_lshl_b64 s[0:1], s[0:1], 11
	s_add_u32 s2, s0, s18
	s_waitcnt lgkmcnt(0)
	v_add_f32_e32 v66, v64, v65
	s_addc_u32 s3, s1, s67
	v_div_scale_f32 v67, s[0:1], v66, v66, 1.0
	v_rcp_f32_e32 v68, v67
	v_mov_b32_e32 v65, s3
	v_or_b32_e32 v64, s2, v170
	v_lshl_add_u64 v[64:65], v[64:65], 0, s[24:25]
	v_fma_f32 v69, -v67, v68, 1.0
	v_fmac_f32_e32 v68, v69, v68
	v_div_scale_f32 v69, vcc, 1.0, v66, 1.0
	v_mul_f32_e32 v70, v69, v68
	v_fma_f32 v71, -v67, v70, v69
	v_fmac_f32_e32 v70, v71, v68
	v_fma_f32 v67, -v67, v70, v69
	v_div_fmas_f32 v67, v67, v68, v70
	v_lshlrev_b64 v[64:65], 12, v[64:65]
	s_lshl_b32 s0, s22, 8
	v_div_fixup_f32 v66, v67, v66, 1.0
	v_lshl_add_u64 v[64:65], s[16:17], 0, v[64:65]
	s_and_b32 s18, s0, 0x700
	v_lshl_add_u64 v[64:65], v[64:65], 0, s[18:19]
	v_mov_b32_e32 v81, v163
	v_lshl_add_u64 v[64:65], v[80:81], 1, v[64:65]
	v_mbcnt_lo_u32_b32 v67, -1, 0
	v_mbcnt_hi_u32_b32 v67, -1, v67
	v_and_b32_e32 v67, 32, v67
	v_lshrrev_b32_e32 v68, 2, v67
	v_mov_b32_e32 v69, 0
	v_lshl_add_u64 v[64:65], v[64:65], 0, v[68:69]
	v_pk_mul_f32 v[48:49], v[48:49], v[66:67] op_sel_hi:[1,0]
	v_pk_mul_f32 v[50:51], v[50:51], v[66:67] op_sel_hi:[1,0]
	v_pk_mul_f32 v[52:53], v[52:53], v[66:67] op_sel_hi:[1,0]
	v_pk_mul_f32 v[54:55], v[54:55], v[66:67] op_sel_hi:[1,0]
	v_cvt_pk_bf16_f32 v48, v48, v49
	v_cvt_pk_bf16_f32 v49, v50, v51
	v_cvt_pk_bf16_f32 v50, v52, v53
	v_cvt_pk_bf16_f32 v51, v54, v55
	s_nop 1
	v_permlane32_swap_b32_e32 v48, v50
	v_permlane32_swap_b32_e32 v49, v51
	global_store_dwordx4 v[64:65], v[48:51], off
	v_pk_mul_f32 v[56:57], v[56:57], v[66:67] op_sel_hi:[1,0]
	v_pk_mul_f32 v[58:59], v[58:59], v[66:67] op_sel_hi:[1,0]
	v_pk_mul_f32 v[60:61], v[60:61], v[66:67] op_sel_hi:[1,0]
	v_pk_mul_f32 v[62:63], v[62:63], v[66:67] op_sel_hi:[1,0]
	v_cvt_pk_bf16_f32 v56, v56, v57
	v_cvt_pk_bf16_f32 v57, v58, v59
	v_cvt_pk_bf16_f32 v58, v60, v61
	v_cvt_pk_bf16_f32 v59, v62, v63
	s_nop 1
	v_permlane32_swap_b32_e32 v56, v58
	v_permlane32_swap_b32_e32 v57, v59
	global_store_dwordx4 v[64:65], v[56:59], off offset:32
	v_pk_mul_f32 v[32:33], v[32:33], v[66:67] op_sel_hi:[1,0]
	v_pk_mul_f32 v[34:35], v[34:35], v[66:67] op_sel_hi:[1,0]
	v_pk_mul_f32 v[36:37], v[36:37], v[66:67] op_sel_hi:[1,0]
	v_pk_mul_f32 v[38:39], v[38:39], v[66:67] op_sel_hi:[1,0]
	v_cvt_pk_bf16_f32 v32, v32, v33
	v_cvt_pk_bf16_f32 v33, v34, v35
	v_cvt_pk_bf16_f32 v34, v36, v37
	v_cvt_pk_bf16_f32 v35, v38, v39
	s_nop 1
	v_permlane32_swap_b32_e32 v32, v34
	v_permlane32_swap_b32_e32 v33, v35
	global_store_dwordx4 v[64:65], v[32:35], off offset:64
	v_pk_mul_f32 v[40:41], v[40:41], v[66:67] op_sel_hi:[1,0]
	v_pk_mul_f32 v[42:43], v[42:43], v[66:67] op_sel_hi:[1,0]
	v_pk_mul_f32 v[44:45], v[44:45], v[66:67] op_sel_hi:[1,0]
	v_pk_mul_f32 v[46:47], v[46:47], v[66:67] op_sel_hi:[1,0]
	v_cvt_pk_bf16_f32 v40, v40, v41
	v_cvt_pk_bf16_f32 v41, v42, v43
	v_cvt_pk_bf16_f32 v42, v44, v45
	v_cvt_pk_bf16_f32 v43, v46, v47
	s_nop 1
	v_permlane32_swap_b32_e32 v40, v42
	v_permlane32_swap_b32_e32 v41, v43
	global_store_dwordx4 v[64:65], v[40:43], off offset:96
	v_pk_mul_f32 v[16:17], v[16:17], v[66:67] op_sel_hi:[1,0]
	v_pk_mul_f32 v[18:19], v[18:19], v[66:67] op_sel_hi:[1,0]
	v_pk_mul_f32 v[20:21], v[20:21], v[66:67] op_sel_hi:[1,0]
	v_pk_mul_f32 v[22:23], v[22:23], v[66:67] op_sel_hi:[1,0]
	v_cvt_pk_bf16_f32 v16, v16, v17
	v_cvt_pk_bf16_f32 v17, v18, v19
	v_cvt_pk_bf16_f32 v18, v20, v21
	v_cvt_pk_bf16_f32 v19, v22, v23
	s_nop 1
	v_permlane32_swap_b32_e32 v16, v18
	v_permlane32_swap_b32_e32 v17, v19
	global_store_dwordx4 v[64:65], v[16:19], off offset:128
	v_pk_mul_f32 v[24:25], v[24:25], v[66:67] op_sel_hi:[1,0]
	v_pk_mul_f32 v[26:27], v[26:27], v[66:67] op_sel_hi:[1,0]
	v_pk_mul_f32 v[28:29], v[28:29], v[66:67] op_sel_hi:[1,0]
	v_pk_mul_f32 v[30:31], v[30:31], v[66:67] op_sel_hi:[1,0]
	v_cvt_pk_bf16_f32 v24, v24, v25
	v_cvt_pk_bf16_f32 v25, v26, v27
	v_cvt_pk_bf16_f32 v26, v28, v29
	v_cvt_pk_bf16_f32 v27, v30, v31
	s_nop 1
	v_permlane32_swap_b32_e32 v24, v26
	v_permlane32_swap_b32_e32 v25, v27
	global_store_dwordx4 v[64:65], v[24:27], off offset:160
	v_pk_mul_f32 v[0:1], v[0:1], v[66:67] op_sel_hi:[1,0]
	v_pk_mul_f32 v[2:3], v[2:3], v[66:67] op_sel_hi:[1,0]
	v_pk_mul_f32 v[4:5], v[4:5], v[66:67] op_sel_hi:[1,0]
	v_pk_mul_f32 v[6:7], v[6:7], v[66:67] op_sel_hi:[1,0]
	v_cvt_pk_bf16_f32 v0, v0, v1
	v_cvt_pk_bf16_f32 v1, v2, v3
	v_cvt_pk_bf16_f32 v2, v4, v5
	v_cvt_pk_bf16_f32 v3, v6, v7
	s_nop 1
	v_permlane32_swap_b32_e32 v0, v2
	v_permlane32_swap_b32_e32 v1, v3
	global_store_dwordx4 v[64:65], v[0:3], off offset:192
	v_pk_mul_f32 v[8:9], v[8:9], v[66:67] op_sel_hi:[1,0]
	v_pk_mul_f32 v[10:11], v[10:11], v[66:67] op_sel_hi:[1,0]
	v_pk_mul_f32 v[12:13], v[12:13], v[66:67] op_sel_hi:[1,0]
	v_pk_mul_f32 v[14:15], v[14:15], v[66:67] op_sel_hi:[1,0]
	v_cvt_pk_bf16_f32 v8, v8, v9
	v_cvt_pk_bf16_f32 v9, v10, v11
	v_cvt_pk_bf16_f32 v10, v12, v13
	v_cvt_pk_bf16_f32 v11, v14, v15
	s_nop 1
	v_permlane32_swap_b32_e32 v8, v10
	v_permlane32_swap_b32_e32 v9, v11
	global_store_dwordx4 v[64:65], v[8:11], off offset:224
	s_mov_b64 s[0:1], 0
	s_branch .LBB0_657

; __device__ __forceinline__ unsigned cvt_pk_bf16(float lo, float hi) { const bf16x2_t r = __builtin_convertvector((f32x2_t){lo, hi}, bf16x2_t); return __builtin_bit_cast(unsigned, r); }
; __device__ __forceinline__ void attn_unit(LAS unsigned char* lds, const bf16_t* Q, const bf16_t* K, const bf16_t* Vt, const float* kmean, bf16_t* mix,
;                                           const int b, const int h, const int blk, const int wv) {
;     ...
;     lsum += __shfl_xor(lsum, 32);
;     const float inv = 1.0f / lsum;
;     bf16_t* op = mix + qrow * DM + h * 128 + 4 * hh;
; #pragma unroll
;     for (int d = 0; d < 4; ++d)
; #pragma unroll
;         for (int rg = 0; rg < 4; ++rg) {
;             u32x2 wv; wv[0] = cvt_pk_bf16(o[d][4 * rg] * inv, o[d][4 * rg + 1] * inv); wv[1] = cvt_pk_bf16(o[d][4 * rg + 2] * inv, o[d][4 * rg + 3] * inv);
;             *(u32x2*)(op + 32 * d + 8 * rg) = wv;
;         }
.LBB0_1838:
	ds_bpermute_b32 v65, v171, v64
	s_ashr_i32 s0, s22, 3
	s_ashr_i32 s1, s0, 31
	s_lshl_b64 s[0:1], s[0:1], 11
	s_add_u32 s2, s0, s18
	s_waitcnt lgkmcnt(0)
	v_add_f32_e32 v66, v64, v65
	s_addc_u32 s3, s1, s64
	v_div_scale_f32 v67, s[0:1], v66, v66, 1.0
	v_rcp_f32_e32 v68, v67
	v_mov_b32_e32 v65, s3
	v_or_b32_e32 v64, s2, v170
	v_lshl_add_u64 v[64:65], v[64:65], 0, s[24:25]
	v_fma_f32 v69, -v67, v68, 1.0
	v_fmac_f32_e32 v68, v69, v68
	v_div_scale_f32 v69, vcc, 1.0, v66, 1.0
	v_mul_f32_e32 v70, v69, v68
	v_fma_f32 v71, -v67, v70, v69
	v_fmac_f32_e32 v70, v71, v68
	v_fma_f32 v67, -v67, v70, v69
	v_div_fmas_f32 v67, v67, v68, v70
	v_lshlrev_b64 v[64:65], 12, v[64:65]
	s_lshl_b32 s0, s22, 8
	v_div_fixup_f32 v66, v67, v66, 1.0
	v_lshl_add_u64 v[64:65], s[16:17], 0, v[64:65]
	s_and_b32 s18, s0, 0x700
	v_lshl_add_u64 v[64:65], v[64:65], 0, s[18:19]
	v_mov_b32_e32 v81, v163
	v_lshl_add_u64 v[64:65], v[80:81], 1, v[64:65]
	v_mbcnt_lo_u32_b32 v67, -1, 0
	v_mbcnt_hi_u32_b32 v67, -1, v67
	v_and_b32_e32 v67, 32, v67
	v_lshrrev_b32_e32 v68, 2, v67
	v_mov_b32_e32 v69, 0
	v_lshl_add_u64 v[64:65], v[64:65], 0, v[68:69]
	v_pk_mul_f32 v[48:49], v[48:49], v[66:67] op_sel_hi:[1,0]
	v_pk_mul_f32 v[50:51], v[50:51], v[66:67] op_sel_hi:[1,0]
	v_pk_mul_f32 v[52:53], v[52:53], v[66:67] op_sel_hi:[1,0]
	v_pk_mul_f32 v[54:55], v[54:55], v[66:67] op_sel_hi:[1,0]
	v_cvt_pk_bf16_f32 v48, v48, v49
	v_cvt_pk_bf16_f32 v49, v50, v51
	v_cvt_pk_bf16_f32 v50, v52, v53
	v_cvt_pk_bf16_f32 v51, v54, v55
	s_nop 1
	v_permlane32_swap_b32_e32 v48, v50
	v_permlane32_swap_b32_e32 v49, v51
	global_store_dwordx4 v[64:65], v[48:51], off
	v_pk_mul_f32 v[56:57], v[56:57], v[66:67] op_sel_hi:[1,0]
	v_pk_mul_f32 v[58:59], v[58:59], v[66:67] op_sel_hi:[1,0]
	v_pk_mul_f32 v[60:61], v[60:61], v[66:67] op_sel_hi:[1,0]
	v_pk_mul_f32 v[62:63], v[62:63], v[66:67] op_sel_hi:[1,0]
	v_cvt_pk_bf16_f32 v56, v56, v57
	v_cvt_pk_bf16_f32 v57, v58, v59
	v_cvt_pk_bf16_f32 v58, v60, v61
	v_cvt_pk_bf16_f32 v59, v62, v63
	s_nop 1
	v_permlane32_swap_b32_e32 v56, v58
	v_permlane32_swap_b32_e32 v57, v59
	global_store_dwordx4 v[64:65], v[56:59], off offset:32
	v_pk_mul_f32 v[32:33], v[32:33], v[66:67] op_sel_hi:[1,0]
	v_pk_mul_f32 v[34:35], v[34:35], v[66:67] op_sel_hi:[1,0]
	v_pk_mul_f32 v[36:37], v[36:37], v[66:67] op_sel_hi:[1,0]
	v_pk_mul_f32 v[38:39], v[38:39], v[66:67] op_sel_hi:[1,0]
	v_cvt_pk_bf16_f32 v32, v32, v33
	v_cvt_pk_bf16_f32 v33, v34, v35
	v_cvt_pk_bf16_f32 v34, v36, v37
	v_cvt_pk_bf16_f32 v35, v38, v39
	s_nop 1
	v_permlane32_swap_b32_e32 v32, v34
	v_permlane32_swap_b32_e32 v33, v35
	global_store_dwordx4 v[64:65], v[32:35], off offset:64
	v_pk_mul_f32 v[40:41], v[40:41], v[66:67] op_sel_hi:[1,0]
	v_pk_mul_f32 v[42:43], v[42:43], v[66:67] op_sel_hi:[1,0]
	v_pk_mul_f32 v[44:45], v[44:45], v[66:67] op_sel_hi:[1,0]
	v_pk_mul_f32 v[46:47], v[46:47], v[66:67] op_sel_hi:[1,0]
	v_cvt_pk_bf16_f32 v40, v40, v41
	v_cvt_pk_bf16_f32 v41, v42, v43
	v_cvt_pk_bf16_f32 v42, v44, v45
	v_cvt_pk_bf16_f32 v43, v46, v47
	s_nop 1
	v_permlane32_swap_b32_e32 v40, v42
	v_permlane32_swap_b32_e32 v41, v43
	global_store_dwordx4 v[64:65], v[40:43], off offset:96
	v_pk_mul_f32 v[16:17], v[16:17], v[66:67] op_sel_hi:[1,0]
	v_pk_mul_f32 v[18:19], v[18:19], v[66:67] op_sel_hi:[1,0]
	v_pk_mul_f32 v[20:21], v[20:21], v[66:67] op_sel_hi:[1,0]
	v_pk_mul_f32 v[22:23], v[22:23], v[66:67] op_sel_hi:[1,0]
	v_cvt_pk_bf16_f32 v16, v16, v17
	v_cvt_pk_bf16_f32 v17, v18, v19
	v_cvt_pk_bf16_f32 v18, v20, v21
	v_cvt_pk_bf16_f32 v19, v22, v23
	s_nop 1
	v_permlane32_swap_b32_e32 v16, v18
	v_permlane32_swap_b32_e32 v17, v19
	global_store_dwordx4 v[64:65], v[16:19], off offset:128
	v_pk_mul_f32 v[24:25], v[24:25], v[66:67] op_sel_hi:[1,0]
	v_pk_mul_f32 v[26:27], v[26:27], v[66:67] op_sel_hi:[1,0]
	v_pk_mul_f32 v[28:29], v[28:29], v[66:67] op_sel_hi:[1,0]
	v_pk_mul_f32 v[30:31], v[30:31], v[66:67] op_sel_hi:[1,0]
	v_cvt_pk_bf16_f32 v24, v24, v25
	v_cvt_pk_bf16_f32 v25, v26, v27
	v_cvt_pk_bf16_f32 v26, v28, v29
	v_cvt_pk_bf16_f32 v27, v30, v31
	s_nop 1
	v_permlane32_swap_b32_e32 v24, v26
	v_permlane32_swap_b32_e32 v25, v27
	global_store_dwordx4 v[64:65], v[24:27], off offset:160
	v_pk_mul_f32 v[0:1], v[0:1], v[66:67] op_sel_hi:[1,0]
	v_pk_mul_f32 v[2:3], v[2:3], v[66:67] op_sel_hi:[1,0]
	v_pk_mul_f32 v[4:5], v[4:5], v[66:67] op_sel_hi:[1,0]
	v_pk_mul_f32 v[6:7], v[6:7], v[66:67] op_sel_hi:[1,0]
	v_cvt_pk_bf16_f32 v0, v0, v1
	v_cvt_pk_bf16_f32 v1, v2, v3
	v_cvt_pk_bf16_f32 v2, v4, v5
	v_cvt_pk_bf16_f32 v3, v6, v7
	s_nop 1
	v_permlane32_swap_b32_e32 v0, v2
	v_permlane32_swap_b32_e32 v1, v3
	global_store_dwordx4 v[64:65], v[0:3], off offset:192
	v_pk_mul_f32 v[8:9], v[8:9], v[66:67] op_sel_hi:[1,0]
	v_pk_mul_f32 v[10:11], v[10:11], v[66:67] op_sel_hi:[1,0]
	v_pk_mul_f32 v[12:13], v[12:13], v[66:67] op_sel_hi:[1,0]
	v_pk_mul_f32 v[14:15], v[14:15], v[66:67] op_sel_hi:[1,0]
	v_cvt_pk_bf16_f32 v8, v8, v9
	v_cvt_pk_bf16_f32 v9, v10, v11
	v_cvt_pk_bf16_f32 v10, v12, v13
	v_cvt_pk_bf16_f32 v11, v14, v15
	s_nop 1
	v_permlane32_swap_b32_e32 v8, v10
	v_permlane32_swap_b32_e32 v9, v11
	global_store_dwordx4 v[64:65], v[8:11], off offset:224
	s_mov_b64 s[0:1], 0
	s_branch .LBB0_1714
